# waves 4-7 issue their K prefetch after barrier1 instead of before it
# speedup vs baseline: 1.0265x; 1.0041x over previous
.LBB1_13:
	s_waitcnt vmcnt(12)
	v_cvt_pk_f16_f32 v151, v120, v121
	v_cvt_pk_f16_f32 v150, v100, v101
	v_cvt_pk_f16_f32 v149, v98, v99
	v_cvt_pk_f16_f32 v148, v112, v113
	s_add_i32 s24, s57, 1
	s_cmp_lg_u32 s57, 7
	s_waitcnt vmcnt(11)
	v_mfma_f32_32x32x16_f16 v[0:15], v[144:147], v[148:151], v[0:15]
	s_cselect_b32 s59, s24, 7
	s_lshl_b32 s25, s59, 2
	s_and_b32 s25, s25, 56
	s_or_b32 s58, s25, s27
	s_lshl_b32 s25, s55, 5
	s_and_b32 s59, s59, 1
	s_waitcnt vmcnt(10)
	v_mfma_f32_32x32x16_f16 v[16:31], v[140:143], v[148:151], v[16:31]
	v_cvt_pk_f16_f32 v143, v180, v181
	v_cvt_pk_f16_f32 v142, v124, v125
	v_cvt_pk_f16_f32 v141, v122, v123
	v_cvt_pk_f16_f32 v140, v102, v103
	s_waitcnt vmcnt(9)
	s_nop 0
	v_mfma_f32_32x32x16_f16 v[0:15], v[136:139], v[140:143], v[0:15]
	s_waitcnt vmcnt(8)
	v_mfma_f32_32x32x16_f16 v[16:31], v[132:135], v[140:143], v[16:31]
	s_add_i32 s61, s35, s60
	s_and_b32 s61, s61, 0x3f000
	v_or_b32_e32 v144, s61, v248
	s_add_i32 s61, s36, s60
	s_and_b32 s61, s61, 0x3f000
	v_or_b32_e32 v160, s61, v248
	global_load_dwordx4 v[132:135], v144, s[16:17]
	global_load_dwordx4 v[136:139], v144, s[16:17] offset:1024
	global_load_dwordx4 v[140:143], v144, s[16:17] offset:2048
	s_nop 0
	global_load_dwordx4 v[144:147], v144, s[16:17] offset:3072
	s_nop 0
	global_load_dwordx4 v[148:151], v160, s[16:17]
	global_load_dwordx4 v[152:155], v160, s[16:17] offset:1024
	global_load_dwordx4 v[156:159], v160, s[16:17] offset:2048
	s_nop 0
	global_load_dwordx4 v[160:163], v160, s[16:17] offset:3072
	v_cvt_pk_f16_f32 v253, v96, v97
	v_cvt_pk_f16_f32 v252, v84, v85
	v_cvt_pk_f16_f32 v251, v82, v83
	v_cvt_pk_f16_f32 v250, v80, v81
	s_waitcnt vmcnt(15)
	s_nop 0
	v_mfma_f32_32x32x16_f16 v[0:15], v[60:63], v[250:253], v[0:15]
	s_waitcnt vmcnt(14)
	v_mfma_f32_32x32x16_f16 v[16:31], v[56:59], v[250:253], v[16:31]
	v_cvt_pk_f16_f32 v59, v94, v95
	v_cvt_pk_f16_f32 v58, v90, v91
	v_cvt_pk_f16_f32 v57, v88, v89
	v_cvt_pk_f16_f32 v56, v86, v87
	s_waitcnt vmcnt(13)
	s_nop 0
	v_mfma_f32_32x32x16_f16 v[0:15], v[52:55], v[56:59], v[0:15]
	s_waitcnt vmcnt(12)
	v_mfma_f32_32x32x16_f16 v[16:31], v[48:51], v[56:59], v[16:31]
	v_cvt_pk_f16_f32 v51, v176, v177
	v_cvt_pk_f16_f32 v50, v110, v111
	v_cvt_pk_f16_f32 v49, v108, v109
	v_cvt_pk_f16_f32 v48, v92, v93
	s_waitcnt vmcnt(11)
	s_nop 0
	v_mfma_f32_32x32x16_f16 v[0:15], v[44:47], v[48:51], v[0:15]
	s_waitcnt vmcnt(10)
	v_mfma_f32_32x32x16_f16 v[16:31], v[40:43], v[48:51], v[16:31]
	v_cvt_pk_f16_f32 v43, v206, v207
	v_cvt_pk_f16_f32 v42, v194, v195
	v_cvt_pk_f16_f32 v41, v192, v193
	v_cvt_pk_f16_f32 v40, v174, v175
	s_waitcnt vmcnt(9)
	s_nop 0
	v_mfma_f32_32x32x16_f16 v[0:15], v[36:39], v[40:43], v[0:15]
	s_waitcnt vmcnt(8)
	v_mfma_f32_32x32x16_f16 v[16:31], v[32:35], v[40:43], v[16:31]
	s_add_i32 s61, s37, s60
	s_add_i32 s60, s38, s60
	s_and_b32 s61, s61, 0x3f000
	s_and_b32 s60, s60, 0x3f000
	v_or_b32_e32 v44, s61, v248
	v_or_b32_e32 v60, s60, v248
	global_load_dwordx4 v[32:35], v44, s[16:17]
	global_load_dwordx4 v[36:39], v44, s[16:17] offset:1024
	global_load_dwordx4 v[40:43], v44, s[16:17] offset:2048
	s_nop 0
	global_load_dwordx4 v[44:47], v44, s[16:17] offset:3072
	s_nop 0
	global_load_dwordx4 v[48:51], v60, s[16:17]
	global_load_dwordx4 v[52:55], v60, s[16:17] offset:1024
	global_load_dwordx4 v[56:59], v60, s[16:17] offset:2048
	s_nop 0
	global_load_dwordx4 v[60:63], v60, s[16:17] offset:3072
	v_cvt_pk_f16_f32 v251, v74, v75
	v_cvt_pk_f16_f32 v250, v68, v69
	v_cvt_pk_f16_f32 v249, v66, v67
	v_cvt_pk_f16_f32 v248, v64, v65
	s_waitcnt vmcnt(15)
	s_nop 0
	v_mfma_f32_32x32x16_f16 v[0:15], v[132:135], v[248:251], v[0:15]
	v_cvt_pk_f16_f32 v135, v172, v173
	v_cvt_pk_f16_f32 v134, v106, v107
	v_cvt_pk_f16_f32 v133, v104, v105
	v_cvt_pk_f16_f32 v132, v72, v73
	s_waitcnt vmcnt(14)
	v_mfma_f32_32x32x16_f16 v[16:31], v[136:139], v[248:251], v[16:31]
	s_waitcnt vmcnt(13)
	v_mfma_f32_32x32x16_f16 v[0:15], v[140:143], v[132:135], v[0:15]
	s_waitcnt vmcnt(12)
	v_mfma_f32_32x32x16_f16 v[16:31], v[144:147], v[132:135], v[16:31]
	v_cvt_pk_f16_f32 v135, v202, v203
	v_cvt_pk_f16_f32 v134, v190, v191
	v_cvt_pk_f16_f32 v133, v188, v189
	v_cvt_pk_f16_f32 v132, v170, v171
	s_waitcnt vmcnt(11)
	s_nop 0
	v_mfma_f32_32x32x16_f16 v[0:15], v[148:151], v[132:135], v[0:15]
	s_waitcnt vmcnt(10)
	v_mfma_f32_32x32x16_f16 v[16:31], v[152:155], v[132:135], v[16:31]
	v_cvt_pk_f16_f32 v135, v222, v223
	v_cvt_pk_f16_f32 v134, v216, v217
	v_cvt_pk_f16_f32 v133, v214, v215
	v_cvt_pk_f16_f32 v132, v200, v201
	s_waitcnt vmcnt(9)
	s_nop 0
	v_mfma_f32_32x32x16_f16 v[0:15], v[156:159], v[132:135], v[0:15]
	s_waitcnt vmcnt(8)
	v_mfma_f32_32x32x16_f16 v[16:31], v[160:163], v[132:135], v[16:31]
	v_cvt_pk_f16_f32 v135, v168, v169
	v_cvt_pk_f16_f32 v134, v78, v79
	v_cvt_pk_f16_f32 v133, v76, v77
	v_cvt_pk_f16_f32 v132, v70, v71
	s_waitcnt vmcnt(7)
	s_nop 0
	v_mfma_f32_32x32x16_f16 v[0:15], v[32:35], v[132:135], v[0:15]
	v_cvt_pk_f16_f32 v35, v198, v199
	v_cvt_pk_f16_f32 v34, v186, v187
	v_cvt_pk_f16_f32 v33, v184, v185
	v_cvt_pk_f16_f32 v32, v126, v127
	s_waitcnt vmcnt(6)
	v_mfma_f32_32x32x16_f16 v[16:31], v[36:39], v[132:135], v[16:31]
	s_waitcnt vmcnt(5)
	v_mfma_f32_32x32x16_f16 v[0:15], v[40:43], v[32:35], v[0:15]
	s_waitcnt vmcnt(4)
	v_mfma_f32_32x32x16_f16 v[16:31], v[44:47], v[32:35], v[16:31]
	v_cvt_pk_f16_f32 v35, v220, v221
	v_cvt_pk_f16_f32 v34, v212, v213
	v_cvt_pk_f16_f32 v33, v210, v211
	v_cvt_pk_f16_f32 v32, v196, v197
	s_waitcnt vmcnt(3)
	s_nop 0
	v_mfma_f32_32x32x16_f16 v[0:15], v[48:51], v[32:35], v[0:15]
	s_waitcnt vmcnt(2)
	v_mfma_f32_32x32x16_f16 v[16:31], v[52:55], v[32:35], v[16:31]
	v_cvt_pk_f16_f32 v35, v228, v229
	v_cvt_pk_f16_f32 v34, v226, v227
	v_cvt_pk_f16_f32 v33, v224, v225
	v_cvt_pk_f16_f32 v32, v218, v219
	s_waitcnt vmcnt(1)
	s_nop 0
	v_mfma_f32_32x32x16_f16 v[0:15], v[56:59], v[32:35], v[0:15]
	s_waitcnt vmcnt(0)
	v_mfma_f32_32x32x16_f16 v[16:31], v[60:63], v[32:35], v[16:31]
	s_cmp_lt_u32 s31, 0x200
	s_cbranch_scc0 .Lka_late
	s_or_b32 s62, s39, s59
	s_lshl_b32 s62, s62, 12
	s_lshl_b32 s66, s58, 18
	s_and_b32 s63, s62, 0x3f000
	s_or_b32 s63, s63, s66
	v_or_b32_e32 v252, s63, v231
	global_load_dwordx4 v[48:51], v252, s[6:7]
	global_load_dwordx4 v[52:55], v252, s[6:7] offset:1024
	global_load_dwordx4 v[56:59], v252, s[6:7] offset:2048
	global_load_dwordx4 v[60:63], v252, s[6:7] offset:3072
	s_add_i32 s63, s62, 0x4000
	s_and_b32 s63, s63, 0x3f000
	s_or_b32 s63, s63, s66
	v_or_b32_e32 v253, s63, v231
	global_load_dwordx4 v[40:43], v253, s[6:7] offset:2048
	global_load_dwordx4 v[44:47], v253, s[6:7] offset:3072
	s_add_i32 s63, s62, 0x6000
	s_and_b32 s63, s63, 0x3f000
	s_or_b32 s63, s63, s66
	v_or_b32_e32 v252, s63, v231
	global_load_dwordx4 v[148:151], v252, s[6:7] offset:3072
	s_add_i32 s63, s62, 0x7000
	s_and_b32 s63, s63, 0x3f000
	s_or_b32 s63, s63, s66
	v_or_b32_e32 v253, s63, v231
	global_load_dwordx4 v[132:135], v253, s[6:7]
	global_load_dwordx4 v[136:139], v253, s[6:7] offset:1024
	global_load_dwordx4 v[140:143], v253, s[6:7] offset:2048
	global_load_dwordx4 v[144:147], v253, s[6:7] offset:3072
	s_add_i32 s63, s62, 0x1000
	s_and_b32 s63, s63, 0x3f000
	s_or_b32 s63, s63, s66
	v_or_b32_e32 v252, s63, v231
	global_load_dwordx4 v[152:155], v252, s[6:7]
	global_load_dwordx4 v[156:159], v252, s[6:7] offset:1024
.Lka_late:
	s_nop 9
	v_mul_f32_e64 v0, s18, v0
	v_mul_f32_e64 v1, s19, v1
	v_mul_f32_e64 v2, s18, v2
	v_mul_f32_e64 v3, s19, v3
	v_pk_mul_f32 v[16:17], s[18:19], v[16:17]
	v_pk_mul_f32 v[18:19], s[18:19], v[18:19]
	ds_write_b128 v164, v[0:3]
	ds_write_b128 v164, v[16:19] offset:128
	v_pk_mul_f32 v[0:1], s[18:19], v[4:5]
	v_pk_mul_f32 v[2:3], s[18:19], v[6:7]
	v_pk_mul_f32 v[4:5], s[18:19], v[20:21]
	v_pk_mul_f32 v[6:7], s[18:19], v[22:23]
	ds_write_b128 v164, v[0:3] offset:32
	ds_write_b128 v164, v[4:7] offset:160
	v_pk_mul_f32 v[0:1], s[18:19], v[8:9]
	v_pk_mul_f32 v[2:3], s[18:19], v[10:11]
	v_pk_mul_f32 v[4:5], s[18:19], v[24:25]
	v_pk_mul_f32 v[6:7], s[18:19], v[26:27]
	ds_write_b128 v164, v[0:3] offset:64
	ds_write_b128 v164, v[4:7] offset:192
	v_pk_mul_f32 v[0:1], s[18:19], v[12:13]
	v_pk_mul_f32 v[2:3], s[18:19], v[14:15]
	v_pk_mul_f32 v[4:5], s[18:19], v[28:29]
	v_pk_mul_f32 v[6:7], s[18:19], v[30:31]
	ds_write_b128 v164, v[0:3] offset:96
	ds_write_b128 v164, v[4:7] offset:224
	s_waitcnt lgkmcnt(0)
	s_barrier
	s_cmp_lt_u32 s31, 0x200
	s_cbranch_scc1 .Lka_done
	s_or_b32 s62, s39, s59
	s_lshl_b32 s62, s62, 12
	s_lshl_b32 s66, s58, 18
	s_and_b32 s63, s62, 0x3f000
	s_or_b32 s63, s63, s66
	v_or_b32_e32 v252, s63, v231
	global_load_dwordx4 v[48:51], v252, s[6:7]
	global_load_dwordx4 v[52:55], v252, s[6:7] offset:1024
	global_load_dwordx4 v[56:59], v252, s[6:7] offset:2048
	global_load_dwordx4 v[60:63], v252, s[6:7] offset:3072
	s_add_i32 s63, s62, 0x4000
	s_and_b32 s63, s63, 0x3f000
	s_or_b32 s63, s63, s66
	v_or_b32_e32 v253, s63, v231
	global_load_dwordx4 v[40:43], v253, s[6:7] offset:2048
	global_load_dwordx4 v[44:47], v253, s[6:7] offset:3072
	s_add_i32 s63, s62, 0x6000
	s_and_b32 s63, s63, 0x3f000
	s_or_b32 s63, s63, s66
	v_or_b32_e32 v252, s63, v231
	global_load_dwordx4 v[148:151], v252, s[6:7] offset:3072
	s_add_i32 s63, s62, 0x7000
	s_and_b32 s63, s63, 0x3f000
	s_or_b32 s63, s63, s66
	v_or_b32_e32 v253, s63, v231
	global_load_dwordx4 v[132:135], v253, s[6:7]
	global_load_dwordx4 v[136:139], v253, s[6:7] offset:1024
	global_load_dwordx4 v[140:143], v253, s[6:7] offset:2048
	global_load_dwordx4 v[144:147], v253, s[6:7] offset:3072
	s_add_i32 s63, s62, 0x1000
	s_and_b32 s63, s63, 0x3f000
	s_or_b32 s63, s63, s66
	v_or_b32_e32 v252, s63, v231
	global_load_dwordx4 v[152:155], v252, s[6:7]
	global_load_dwordx4 v[156:159], v252, s[6:7] offset:1024
.Lka_done:
	ds_read2_b32 v[0:1], v235 offset1:32
	ds_read2_b32 v[2:3], v235 offset0:64 offset1:96
	ds_read2_b32 v[4:5], v235 offset0:128 offset1:160
	ds_read2_b32 v[6:7], v235 offset0:192 offset1:224
	ds_read2_b32 v[10:11], v236 offset0:128 offset1:160
	ds_read2_b32 v[16:17], v165 offset1:32
	ds_write_b128 v232, v[128:131]
	s_waitcnt lgkmcnt(6)
	v_max_f32_e32 v8, v1, v1
	v_max_f32_e32 v9, v0, v0
	v_max_f32_e32 v8, v9, v8
	s_waitcnt lgkmcnt(5)
	v_max3_f32 v8, v8, v2, v3
	s_waitcnt lgkmcnt(4)
	v_max3_f32 v8, v8, v4, v5
	s_waitcnt lgkmcnt(3)
	v_max3_f32 v14, v8, v6, v7
	ds_read2_b32 v[8:9], v236 offset1:32
	v_sub_f32_e32 v0, v0, v14
	v_sub_f32_e32 v1, v1, v14
	v_exp_f32_e32 v0, v0
	v_exp_f32_e32 v1, v1
	v_sub_f32_e32 v4, v4, v14
	v_sub_f32_e32 v5, v5, v14
	v_exp_f32_e32 v4, v4
	v_exp_f32_e32 v5, v5
	s_waitcnt lgkmcnt(0)
	v_pk_mul_f32 v[0:1], v[8:9], v[0:1]
	ds_read2_b32 v[8:9], v236 offset0:64 offset1:96
	v_sub_f32_e32 v2, v2, v14
	v_sub_f32_e32 v3, v3, v14
	v_exp_f32_e32 v2, v2
	v_exp_f32_e32 v3, v3
	ds_read2_b32 v[12:13], v236 offset0:192 offset1:224
	v_sub_f32_e32 v6, v6, v14
	v_sub_f32_e32 v7, v7, v14
	v_pk_mul_f32 v[18:19], v[10:11], v[4:5]
	v_sub_f32_e32 v4, v247, v14
	ds_read2_b32 v[22:23], v165 offset0:64 offset1:96
	ds_read2_b32 v[24:25], v165 offset0:128 offset1:160
	ds_read2_b32 v[26:27], v165 offset0:192 offset1:224
	v_exp_f32_e32 v6, v6
	v_exp_f32_e32 v7, v7
	v_exp_f32_e32 v34, v4
	v_max_f32_e32 v4, v17, v17
	v_max_f32_e32 v5, v16, v16
	v_add_f32_e32 v0, 0, v0
	s_waitcnt lgkmcnt(4)
	v_pk_mul_f32 v[2:3], v[8:9], v[2:3]
	v_max_f32_e32 v4, v5, v4
	v_add_f32_e32 v0, v0, v1
	s_waitcnt lgkmcnt(2)
	v_max3_f32 v4, v4, v22, v23
	v_add_f32_e32 v0, v0, v2
	s_waitcnt lgkmcnt(1)
	v_max3_f32 v4, v4, v24, v25
	v_add_f32_e32 v0, v0, v3
	v_pk_mul_f32 v[20:21], v[12:13], v[6:7]
	s_waitcnt lgkmcnt(0)
	v_max3_f32 v35, v4, v26, v27
	v_add_f32_e32 v18, v0, v18
	ds_read_b128 v[0:3], v245
	ds_read_b128 v[4:7], v237
	v_sub_f32_e32 v8, v16, v35
	v_exp_f32_e32 v16, v8
	ds_read2_b32 v[28:29], v242 offset1:32
	ds_read_b128 v[8:11], v245 offset:34816
	ds_read_b128 v[12:15], v245 offset:60928
	s_min_u32 s57, s57, 5
	s_waitcnt lgkmcnt(3)
	v_pk_add_f32 v[0:1], v[0:1], v[4:5]
	v_pk_add_f32 v[2:3], v[2:3], v[6:7]
	v_pk_fma_f32 v[30:31], v[16:17], v[0:1], 0 op_sel_hi:[0,1,0]
	v_sub_f32_e32 v0, v17, v35
	v_pk_fma_f32 v[32:33], v[16:17], v[2:3], 0 op_sel_hi:[0,1,0]
	v_exp_f32_e32 v17, v0
	v_add_f32_e32 v0, v18, v19
	v_add_f32_e32 v0, v0, v20
	v_add_f32_e32 v36, v0, v21
	ds_read_b128 v[0:3], v245 offset:8704
	ds_read_b128 v[4:7], v245 offset:17408
	s_waitcnt lgkmcnt(4)
	v_pk_mul_f32 v[18:19], v[28:29], v[16:17]
	v_sub_f32_e32 v16, v22, v35
	v_exp_f32_e32 v16, v16
	v_add_f32_e32 v20, 0, v18
	v_mov_b32_e32 v18, v17
	s_waitcnt lgkmcnt(1)
	v_pk_fma_f32 v[0:1], v[18:19], v[0:1], v[30:31] op_sel_hi:[0,1,1]
	v_pk_fma_f32 v[2:3], v[18:19], v[2:3], v[32:33] op_sel_hi:[0,1,1]
	s_waitcnt lgkmcnt(0)
	v_pk_fma_f32 v[4:5], v[16:17], v[4:5], v[0:1] op_sel_hi:[0,1,1]
	v_sub_f32_e32 v0, v23, v35
	v_pk_fma_f32 v[6:7], v[16:17], v[6:7], v[2:3] op_sel_hi:[0,1,1]
	v_exp_f32_e32 v17, v0
	v_add_f32_e32 v21, v20, v19
	ds_read_b128 v[0:3], v245 offset:26112
	ds_read2_b32 v[18:19], v242 offset0:64 offset1:96
	v_sub_f32_e32 v22, v24, v35
	v_exp_f32_e32 v22, v22
	v_mov_b32_e32 v20, v17
	s_waitcnt lgkmcnt(1)
	v_pk_fma_f32 v[0:1], v[20:21], v[0:1], v[4:5] op_sel_hi:[0,1,1]
	v_pk_fma_f32 v[2:3], v[20:21], v[2:3], v[6:7] op_sel_hi:[0,1,1]
	ds_read2_b32 v[4:5], v242 offset0:128 offset1:160
	v_pk_fma_f32 v[8:9], v[22:23], v[8:9], v[0:1] op_sel_hi:[0,1,1]
	v_sub_f32_e32 v0, v25, v35
	v_pk_fma_f32 v[10:11], v[22:23], v[10:11], v[2:3] op_sel_hi:[0,1,1]
	v_exp_f32_e32 v23, v0
	s_waitcnt lgkmcnt(1)
	v_pk_mul_f32 v[0:1], v[18:19], v[16:17]
	s_lshl_b32 s58, s58, 18
	v_add_f32_e32 v0, v21, v0
	v_add_f32_e32 v2, v0, v1
	s_waitcnt lgkmcnt(0)
	v_pk_mul_f32 v[0:1], v[4:5], v[22:23]
	v_sub_f32_e32 v4, v26, v35
	v_add_f32_e32 v0, v2, v0
	v_add_f32_e32 v17, v0, v1
	ds_read_b128 v[0:3], v245 offset:43520
	v_exp_f32_e32 v18, v4
	ds_read2_b32 v[20:21], v242 offset0:192 offset1:224
	v_sub_f32_e32 v4, v27, v35
	v_exp_f32_e32 v19, v4
	ds_read_b128 v[4:7], v245 offset:52224
	v_mov_b32_e32 v16, v23
	s_waitcnt lgkmcnt(2)
	v_pk_fma_f32 v[0:1], v[16:17], v[0:1], v[8:9] op_sel_hi:[0,1,1]
	s_waitcnt lgkmcnt(1)
	v_pk_mul_f32 v[8:9], v[20:21], v[18:19]
	v_pk_fma_f32 v[2:3], v[16:17], v[2:3], v[10:11] op_sel_hi:[0,1,1]
	v_add_f32_e32 v8, v17, v8
	v_add_f32_e32 v8, v8, v9
	s_waitcnt lgkmcnt(0)
	v_pk_fma_f32 v[0:1], v[18:19], v[4:5], v[0:1] op_sel_hi:[0,1,1]
	v_div_scale_f32 v5, s[60:61], v8, v8, 1.0
	v_pk_fma_f32 v[2:3], v[18:19], v[6:7], v[2:3] op_sel_hi:[0,1,1]
	v_rcp_f32_e32 v6, v5
	v_mov_b32_e32 v4, v19
	v_pk_fma_f32 v[2:3], v[4:5], v[14:15], v[2:3] op_sel_hi:[0,1,1]
	v_pk_fma_f32 v[0:1], v[4:5], v[12:13], v[0:1] op_sel_hi:[0,1,1]
	v_fma_f32 v4, -v5, v6, 1.0
	v_fmac_f32_e32 v6, v4, v6
	v_div_scale_f32 v4, vcc, 1.0, v8, 1.0
	v_mul_f32_e32 v7, v4, v6
	v_fma_f32 v9, -v5, v7, v4
	v_fmac_f32_e32 v7, v9, v6
	v_fma_f32 v4, -v5, v7, v4
	v_div_fmas_f32 v4, v4, v6, v7
	s_lshl_b32 s60, s56, 19
	s_lshl_b32 s61, s55, 13
	v_div_fixup_f32 v4, v4, v8, 1.0
	s_add_i32 s60, s60, s61
	v_pk_mul_f32 v[2:3], v[2:3], v[4:5] op_sel_hi:[1,0]
	v_pk_mul_f32 v[0:1], v[0:1], v[4:5] op_sel_hi:[1,0]
	v_or_b32_e32 v4, s60, v230
	s_lshl_b32 s60, s57, 2
	s_add_i32 s60, s60, 8
	s_and_b32 s60, s60, 56
	s_and_b32 s57, s57, 1
	s_or_b32 s60, s60, s27
	s_or_b32 s57, s57, s28
	s_lshl_b32 s60, s60, 19
	s_lshl_b32 s57, s57, 13
	s_add_i32 s60, s60, s57
	s_or_b32 s62, s39, s59
	s_lshl_b32 s62, s62, 12
	global_store_dwordx4 v4, v[0:3], s[8:9] nt
	v_mov_b32_e32 v252, v34
	v_mov_b32_e32 v253, v36
	v_or_b32_e32 v0, s60, v230
	s_barrier
	global_load_dwordx4 v[128:131], v0, s[4:5]
	s_add_i32 s63, s62, 0x4000
	s_and_b32 s63, s63, 0x3f000
	s_or_b32 s63, s63, s58
	v_or_b32_e32 v2, s63, v231
	global_load_dwordx4 v[32:35], v2, s[6:7]
	global_load_dwordx4 v[36:39], v2, s[6:7] offset:1024
	s_add_i32 s63, s62, 0x5000
	s_and_b32 s63, s63, 0x3f000
	s_or_b32 s63, s63, s58
	v_or_b32_e32 v3, s63, v231
	global_load_dwordx4 v[16:19], v3, s[6:7]
	global_load_dwordx4 v[20:23], v3, s[6:7] offset:1024
	global_load_dwordx4 v[24:27], v3, s[6:7] offset:2048
	global_load_dwordx4 v[28:31], v3, s[6:7] offset:3072
	s_add_i32 s63, s62, 0x6000
	s_and_b32 s63, s63, 0x3f000
	s_or_b32 s63, s63, s58
	v_or_b32_e32 v2, s63, v231
	global_load_dwordx4 v[4:7], v2, s[6:7]
	global_load_dwordx4 v[8:11], v2, s[6:7] offset:1024
	global_load_dwordx4 v[12:15], v2, s[6:7] offset:2048
	v_div_scale_f32 v1, s[64:65], v253, v253, v252
	v_rcp_f32_e32 v2, v1
	s_nop 0
	v_fma_f32 v0, -v1, v2, 1.0
	v_fmac_f32_e32 v2, v0, v2
	v_div_scale_f32 v0, vcc, v252, v253, v252
	v_mul_f32_e32 v3, v0, v2
	v_fma_f32 v248, -v1, v3, v0
	v_fmac_f32_e32 v3, v248, v2
	v_fma_f32 v0, -v1, v3, v0
	v_div_fmas_f32 v0, v0, v2, v3
	v_div_fixup_f32 v1, v0, v253, v252
	v_mul_f32_e32 v0, s18, v1
	v_mov_b32_e32 v2, s26
	v_mov_b32_e32 v3, s23
	v_cmp_eq_u32_e64 s[64:65], 0, v233
	v_cmp_eq_u32_e64 s[66:67], 1, v233
	v_cmp_eq_u32_e64 s[68:69], 2, v233
	v_cmp_eq_u32_e64 s[70:71], 3, v233
	v_cndmask_b32_e64 v248, v2, v3, s[64:65]
	v_cndmask_b32_e64 v249, v2, v3, s[66:67]
	v_cndmask_b32_e64 v250, v2, v3, s[68:69]
	v_cndmask_b32_e64 v251, v2, v3, s[70:71]
	v_mul_f32_e32 v248, v1, v248
	v_mul_f32_e32 v249, v1, v249
	v_mul_f32_e32 v250, v1, v250
	v_mul_f32_e32 v251, v1, v251
	v_cndmask_b32_e64 v248, v0, v248, s[2:3]
	v_cndmask_b32_e64 v249, v0, v249, s[2:3]
	v_cndmask_b32_e64 v250, v0, v250, s[2:3]
	v_cndmask_b32_e64 v251, v0, v251, s[2:3]
	v_mul_f32_e32 v248, v248, v208
	v_mul_f32_e32 v249, v249, v209
	v_mul_f32_e32 v250, v250, v204
	v_mul_f32_e32 v251, v251, v205
	ds_write_b128 v238, v[248:251]
	v_cmp_eq_u32_e64 s[64:65], 4, v233
	v_cmp_eq_u32_e64 s[66:67], 5, v233
	v_cmp_eq_u32_e64 s[68:69], 6, v233
	v_cmp_eq_u32_e64 s[70:71], 7, v233
	v_cndmask_b32_e64 v248, v2, v3, s[64:65]
	v_cndmask_b32_e64 v249, v2, v3, s[66:67]
	v_cndmask_b32_e64 v250, v2, v3, s[68:69]
	v_cndmask_b32_e64 v251, v2, v3, s[70:71]
	v_mul_f32_e32 v248, v1, v248
	v_mul_f32_e32 v249, v1, v249
	v_mul_f32_e32 v250, v1, v250
	v_mul_f32_e32 v251, v1, v251
	v_cndmask_b32_e64 v248, v0, v248, s[2:3]
	v_cndmask_b32_e64 v249, v0, v249, s[2:3]
	v_cndmask_b32_e64 v250, v0, v250, s[2:3]
	v_cndmask_b32_e64 v251, v0, v251, s[2:3]
	v_mul_f32_e32 v248, v248, v182
	v_mul_f32_e32 v249, v249, v183
	v_mul_f32_e32 v250, v250, v178
	v_mul_f32_e32 v251, v251, v179
	ds_write_b128 v238, v[248:251] offset:32
	v_cmp_eq_u32_e64 s[64:65], 8, v233
	v_cmp_eq_u32_e64 s[66:67], 9, v233
	v_cmp_eq_u32_e64 s[68:69], 10, v233
	v_cmp_eq_u32_e64 s[70:71], 11, v233
	v_cndmask_b32_e64 v248, v2, v3, s[64:65]
	v_cndmask_b32_e64 v249, v2, v3, s[66:67]
	v_cndmask_b32_e64 v250, v2, v3, s[68:69]
	v_cndmask_b32_e64 v251, v2, v3, s[70:71]
	v_mul_f32_e32 v248, v1, v248
	v_mul_f32_e32 v249, v1, v249
	v_mul_f32_e32 v250, v1, v250
	v_mul_f32_e32 v251, v1, v251
	v_cndmask_b32_e64 v248, v0, v248, s[2:3]
	v_cndmask_b32_e64 v249, v0, v249, s[2:3]
	v_cndmask_b32_e64 v250, v0, v250, s[2:3]
	v_cndmask_b32_e64 v251, v0, v251, s[2:3]
	v_mul_f32_e32 v248, v248, v166
	v_mul_f32_e32 v249, v249, v167
	v_mul_f32_e32 v250, v250, v118
	v_mul_f32_e32 v251, v251, v119
	ds_write_b128 v238, v[248:251] offset:64
	v_cmp_eq_u32_e64 s[64:65], 12, v233
	v_cmp_eq_u32_e64 s[66:67], 13, v233
	v_cmp_eq_u32_e64 s[68:69], 14, v233
	v_cmp_eq_u32_e64 s[70:71], 15, v233
	v_cndmask_b32_e64 v248, v2, v3, s[64:65]
	v_cndmask_b32_e64 v249, v2, v3, s[66:67]
	v_cndmask_b32_e64 v250, v2, v3, s[68:69]
	v_cndmask_b32_e64 v251, v2, v3, s[70:71]
	v_mul_f32_e32 v248, v1, v248
	v_mul_f32_e32 v249, v1, v249
	v_mul_f32_e32 v250, v1, v250
	v_mul_f32_e32 v251, v1, v251
	v_cndmask_b32_e64 v248, v0, v248, s[2:3]
	v_cndmask_b32_e64 v249, v0, v249, s[2:3]
	v_cndmask_b32_e64 v250, v0, v250, s[2:3]
	v_cndmask_b32_e64 v251, v0, v251, s[2:3]
	v_mul_f32_e32 v248, v248, v116
	v_mul_f32_e32 v249, v249, v117
	v_mul_f32_e32 v250, v250, v114
	v_mul_f32_e32 v251, v251, v115
	ds_write_b128 v238, v[248:251] offset:96
	v_pk_mul_f32 v[248:249], v[0:1], v[112:113] op_sel_hi:[0,1]
	v_pk_mul_f32 v[250:251], v[0:1], v[98:99] op_sel_hi:[0,1]
	ds_write_b128 v238, v[248:251] offset:128
	v_pk_mul_f32 v[248:249], v[0:1], v[100:101] op_sel_hi:[0,1]
	v_pk_mul_f32 v[250:251], v[0:1], v[120:121] op_sel_hi:[0,1]
	ds_write_b128 v238, v[248:251] offset:160
	v_pk_mul_f32 v[248:249], v[0:1], v[102:103] op_sel_hi:[0,1]
	v_pk_mul_f32 v[250:251], v[0:1], v[122:123] op_sel_hi:[0,1]
	ds_write_b128 v238, v[248:251] offset:192
	v_pk_mul_f32 v[248:249], v[0:1], v[124:125] op_sel_hi:[0,1]
	v_pk_mul_f32 v[250:251], v[0:1], v[180:181] op_sel_hi:[0,1]
	ds_write_b128 v238, v[248:251] offset:224
	s_lshl_b32 s56, s56, 11
	s_add_i32 s56, s56, s25
	v_or_b32_e32 v252, s56, v239
	v_add_lshl_u32 v253, v241, s55, 7
	v_lshl_or_b32 v1, v252, 13, v240
	v_and_or_b32 v2, v253, s54, v1
	ds_read_b128 v[248:251], v246
	ds_read_b128 v[160:163], v246 offset:1088
	s_waitcnt lgkmcnt(1)
	global_store_dwordx4 v2, v[248:251], s[10:11] nt
	s_nop 0
	ds_read_b128 v[248:251], v246 offset:2176
	v_or_b32_e32 v3, 0x8000, v2
	s_waitcnt lgkmcnt(1)
	global_store_dwordx4 v3, v[160:163], s[10:11] nt
	s_nop 0
	ds_read_b128 v[160:163], v246 offset:3264
	v_or_b32_e32 v252, 0x10000, v2
	s_waitcnt lgkmcnt(1)
	global_store_dwordx4 v252, v[248:251], s[10:11] nt
	s_nop 0
	ds_read_b128 v[248:251], v246 offset:4352
	v_or_b32_e32 v3, 0x18000, v2
	s_waitcnt lgkmcnt(1)
	global_store_dwordx4 v3, v[160:163], s[10:11] nt
	s_nop 0
	ds_read_b128 v[160:163], v246 offset:5440
	v_or_b32_e32 v252, 0x20000, v2
	s_waitcnt lgkmcnt(1)
	global_store_dwordx4 v252, v[248:251], s[10:11] nt
	s_nop 0
	ds_read_b128 v[248:251], v246 offset:6528
	v_or_b32_e32 v3, 0x28000, v2
	s_waitcnt lgkmcnt(1)
	global_store_dwordx4 v3, v[160:163], s[10:11] nt
	s_nop 0
	ds_read_b128 v[160:163], v246 offset:7616
	v_or_b32_e32 v252, 0x30000, v2
	s_waitcnt lgkmcnt(1)
	global_store_dwordx4 v252, v[248:251], s[10:11] nt
	v_or_b32_e32 v3, 0x38000, v2
	s_waitcnt lgkmcnt(0)
	global_store_dwordx4 v3, v[160:163], s[10:11] nt
	v_pk_mul_f32 v[248:249], v[0:1], v[80:81] op_sel_hi:[0,1]
	v_pk_mul_f32 v[250:251], v[0:1], v[82:83] op_sel_hi:[0,1]
	ds_write_b128 v238, v[248:251]
	v_pk_mul_f32 v[248:249], v[0:1], v[84:85] op_sel_hi:[0,1]
	v_pk_mul_f32 v[250:251], v[0:1], v[96:97] op_sel_hi:[0,1]
	ds_write_b128 v238, v[248:251] offset:32
	v_pk_mul_f32 v[248:249], v[0:1], v[86:87] op_sel_hi:[0,1]
	v_pk_mul_f32 v[250:251], v[0:1], v[88:89] op_sel_hi:[0,1]
	ds_write_b128 v238, v[248:251] offset:64
	v_pk_mul_f32 v[248:249], v[0:1], v[90:91] op_sel_hi:[0,1]
	v_pk_mul_f32 v[250:251], v[0:1], v[94:95] op_sel_hi:[0,1]
	ds_write_b128 v238, v[248:251] offset:96
	v_pk_mul_f32 v[248:249], v[0:1], v[92:93] op_sel_hi:[0,1]
	v_pk_mul_f32 v[250:251], v[0:1], v[108:109] op_sel_hi:[0,1]
	ds_write_b128 v238, v[248:251] offset:128
	v_pk_mul_f32 v[248:249], v[0:1], v[110:111] op_sel_hi:[0,1]
	v_pk_mul_f32 v[250:251], v[0:1], v[176:177] op_sel_hi:[0,1]
	ds_write_b128 v238, v[248:251] offset:160
	v_pk_mul_f32 v[248:249], v[0:1], v[174:175] op_sel_hi:[0,1]
	v_pk_mul_f32 v[250:251], v[0:1], v[192:193] op_sel_hi:[0,1]
	ds_write_b128 v238, v[248:251] offset:192
	v_pk_mul_f32 v[248:249], v[0:1], v[194:195] op_sel_hi:[0,1]
	v_pk_mul_f32 v[250:251], v[0:1], v[206:207] op_sel_hi:[0,1]
	ds_write_b128 v238, v[248:251] offset:224
	v_add_u32_e32 v252, 0x100, v253
	v_and_or_b32 v2, v252, s54, v1
	ds_read_b128 v[248:251], v246
	ds_read_b128 v[160:163], v246 offset:1088
	s_waitcnt lgkmcnt(1)
	global_store_dwordx4 v2, v[248:251], s[10:11] nt
	s_nop 0
	ds_read_b128 v[248:251], v246 offset:2176
	v_or_b32_e32 v3, 0x8000, v2
	s_waitcnt lgkmcnt(1)
	global_store_dwordx4 v3, v[160:163], s[10:11] nt
	s_nop 0
	ds_read_b128 v[160:163], v246 offset:3264
	v_or_b32_e32 v252, 0x10000, v2
	s_waitcnt lgkmcnt(1)
	global_store_dwordx4 v252, v[248:251], s[10:11] nt
	s_nop 0
	ds_read_b128 v[248:251], v246 offset:4352
	v_or_b32_e32 v3, 0x18000, v2
	s_waitcnt lgkmcnt(1)
	global_store_dwordx4 v3, v[160:163], s[10:11] nt
	s_nop 0
	ds_read_b128 v[160:163], v246 offset:5440
	v_or_b32_e32 v252, 0x20000, v2
	s_waitcnt lgkmcnt(1)
	global_store_dwordx4 v252, v[248:251], s[10:11] nt
	s_nop 0
	ds_read_b128 v[248:251], v246 offset:6528
	v_or_b32_e32 v3, 0x28000, v2
	s_waitcnt lgkmcnt(1)
	global_store_dwordx4 v3, v[160:163], s[10:11] nt
	s_nop 0
	ds_read_b128 v[160:163], v246 offset:7616
	v_or_b32_e32 v252, 0x30000, v2
	s_waitcnt lgkmcnt(1)
	global_store_dwordx4 v252, v[248:251], s[10:11] nt
	v_or_b32_e32 v3, 0x38000, v2
	s_waitcnt lgkmcnt(0)
	global_store_dwordx4 v3, v[160:163], s[10:11] nt
	s_add_i32 s63, s62, 0x3000
	s_and_b32 s63, s63, 0x3f000
	s_or_b32 s63, s63, s58
	v_or_b32_e32 v2, s63, v231
	global_load_dwordx4 v[80:83], v2, s[6:7]
	global_load_dwordx4 v[84:87], v2, s[6:7] offset:1024
	global_load_dwordx4 v[88:91], v2, s[6:7] offset:2048
	global_load_dwordx4 v[92:95], v2, s[6:7] offset:3072
	s_add_i32 s63, s62, 0x2000
	s_and_b32 s63, s63, 0x3f000
	s_or_b32 s63, s63, s58
	v_or_b32_e32 v3, s63, v231
	global_load_dwordx4 v[96:99], v3, s[6:7]
	global_load_dwordx4 v[100:103], v3, s[6:7] offset:1024
	global_load_dwordx4 v[108:111], v3, s[6:7] offset:2048
	global_load_dwordx4 v[192:195], v3, s[6:7] offset:3072
	s_add_i32 s63, s62, 0x1000
	s_and_b32 s63, s63, 0x3f000
	s_or_b32 s63, s63, s58
	v_or_b32_e32 v2, s63, v231
	global_load_dwordx4 v[174:177], v2, s[6:7] offset:2048
	global_load_dwordx4 v[178:181], v2, s[6:7] offset:3072
	v_pk_mul_f32 v[248:249], v[0:1], v[64:65] op_sel_hi:[0,1]
	v_pk_mul_f32 v[250:251], v[0:1], v[66:67] op_sel_hi:[0,1]
	ds_write_b128 v238, v[248:251]
	v_pk_mul_f32 v[248:249], v[0:1], v[68:69] op_sel_hi:[0,1]
	v_pk_mul_f32 v[250:251], v[0:1], v[74:75] op_sel_hi:[0,1]
	ds_write_b128 v238, v[248:251] offset:32
	v_pk_mul_f32 v[248:249], v[0:1], v[72:73] op_sel_hi:[0,1]
	v_pk_mul_f32 v[250:251], v[0:1], v[104:105] op_sel_hi:[0,1]
	ds_write_b128 v238, v[248:251] offset:64
	v_pk_mul_f32 v[248:249], v[0:1], v[106:107] op_sel_hi:[0,1]
	v_pk_mul_f32 v[250:251], v[0:1], v[172:173] op_sel_hi:[0,1]
	ds_write_b128 v238, v[248:251] offset:96
	v_pk_mul_f32 v[248:249], v[0:1], v[170:171] op_sel_hi:[0,1]
	v_pk_mul_f32 v[250:251], v[0:1], v[188:189] op_sel_hi:[0,1]
	ds_write_b128 v238, v[248:251] offset:128
	v_pk_mul_f32 v[248:249], v[0:1], v[190:191] op_sel_hi:[0,1]
	v_pk_mul_f32 v[250:251], v[0:1], v[202:203] op_sel_hi:[0,1]
	ds_write_b128 v238, v[248:251] offset:160
	v_pk_mul_f32 v[248:249], v[0:1], v[200:201] op_sel_hi:[0,1]
	v_pk_mul_f32 v[250:251], v[0:1], v[214:215] op_sel_hi:[0,1]
	ds_write_b128 v238, v[248:251] offset:192
	v_pk_mul_f32 v[248:249], v[0:1], v[216:217] op_sel_hi:[0,1]
	v_pk_mul_f32 v[250:251], v[0:1], v[222:223] op_sel_hi:[0,1]
	ds_write_b128 v238, v[248:251] offset:224
	v_add_u32_e32 v252, 0x200, v253
	v_and_or_b32 v2, v252, s54, v1
	ds_read_b128 v[248:251], v246
	ds_read_b128 v[160:163], v246 offset:1088
	s_waitcnt lgkmcnt(1)
	global_store_dwordx4 v2, v[248:251], s[10:11] nt
	s_nop 0
	ds_read_b128 v[248:251], v246 offset:2176
	v_or_b32_e32 v3, 0x8000, v2
	s_waitcnt lgkmcnt(1)
	global_store_dwordx4 v3, v[160:163], s[10:11] nt
	s_nop 0
	ds_read_b128 v[160:163], v246 offset:3264
	v_or_b32_e32 v252, 0x10000, v2
	s_waitcnt lgkmcnt(1)
	global_store_dwordx4 v252, v[248:251], s[10:11] nt
	s_nop 0
	ds_read_b128 v[248:251], v246 offset:4352
	v_or_b32_e32 v3, 0x18000, v2
	s_waitcnt lgkmcnt(1)
	global_store_dwordx4 v3, v[160:163], s[10:11] nt
	s_nop 0
	ds_read_b128 v[160:163], v246 offset:5440
	v_or_b32_e32 v252, 0x20000, v2
	s_waitcnt lgkmcnt(1)
	global_store_dwordx4 v252, v[248:251], s[10:11] nt
	s_nop 0
	ds_read_b128 v[248:251], v246 offset:6528
	v_or_b32_e32 v3, 0x28000, v2
	s_waitcnt lgkmcnt(1)
	global_store_dwordx4 v3, v[160:163], s[10:11] nt
	s_nop 0
	ds_read_b128 v[160:163], v246 offset:7616
	v_or_b32_e32 v252, 0x30000, v2
	s_waitcnt lgkmcnt(1)
	global_store_dwordx4 v252, v[248:251], s[10:11] nt
	v_or_b32_e32 v3, 0x38000, v2
	s_waitcnt lgkmcnt(0)
	global_store_dwordx4 v3, v[160:163], s[10:11] nt
	v_pk_mul_f32 v[248:249], v[0:1], v[70:71] op_sel_hi:[0,1]
	v_pk_mul_f32 v[250:251], v[0:1], v[76:77] op_sel_hi:[0,1]
	ds_write_b128 v238, v[248:251]
	v_pk_mul_f32 v[248:249], v[0:1], v[78:79] op_sel_hi:[0,1]
	v_pk_mul_f32 v[250:251], v[0:1], v[168:169] op_sel_hi:[0,1]
	ds_write_b128 v238, v[248:251] offset:32
	v_pk_mul_f32 v[248:249], v[0:1], v[126:127] op_sel_hi:[0,1]
	v_pk_mul_f32 v[250:251], v[0:1], v[184:185] op_sel_hi:[0,1]
	ds_write_b128 v238, v[248:251] offset:64
	v_pk_mul_f32 v[248:249], v[0:1], v[186:187] op_sel_hi:[0,1]
	v_pk_mul_f32 v[250:251], v[0:1], v[198:199] op_sel_hi:[0,1]
	ds_write_b128 v238, v[248:251] offset:96
	v_pk_mul_f32 v[248:249], v[0:1], v[196:197] op_sel_hi:[0,1]
	v_pk_mul_f32 v[250:251], v[0:1], v[210:211] op_sel_hi:[0,1]
	ds_write_b128 v238, v[248:251] offset:128
	v_pk_mul_f32 v[248:249], v[0:1], v[212:213] op_sel_hi:[0,1]
	v_pk_mul_f32 v[250:251], v[0:1], v[220:221] op_sel_hi:[0,1]
	ds_write_b128 v238, v[248:251] offset:160
	v_pk_mul_f32 v[248:249], v[0:1], v[218:219] op_sel_hi:[0,1]
	v_pk_mul_f32 v[250:251], v[0:1], v[224:225] op_sel_hi:[0,1]
	ds_write_b128 v238, v[248:251] offset:192
	v_pk_mul_f32 v[248:249], v[0:1], v[226:227] op_sel_hi:[0,1]
	v_pk_mul_f32 v[250:251], v[0:1], v[228:229] op_sel_hi:[0,1]
	ds_write_b128 v238, v[248:251] offset:224
	v_add_u32_e32 v252, 0x300, v253
	v_and_or_b32 v2, v252, s54, v1
	ds_read_b128 v[248:251], v246
	ds_read_b128 v[160:163], v246 offset:1088
	s_waitcnt lgkmcnt(1)
	global_store_dwordx4 v2, v[248:251], s[10:11] nt
	s_nop 0
	ds_read_b128 v[248:251], v246 offset:2176
	v_or_b32_e32 v3, 0x8000, v2
	s_waitcnt lgkmcnt(1)
	global_store_dwordx4 v3, v[160:163], s[10:11] nt
	s_nop 0
	ds_read_b128 v[160:163], v246 offset:3264
	v_or_b32_e32 v252, 0x10000, v2
	s_waitcnt lgkmcnt(1)
	global_store_dwordx4 v252, v[248:251], s[10:11] nt
	s_nop 0
	ds_read_b128 v[248:251], v246 offset:4352
	v_or_b32_e32 v3, 0x18000, v2
	s_waitcnt lgkmcnt(1)
	global_store_dwordx4 v3, v[160:163], s[10:11] nt
	s_nop 0
	ds_read_b128 v[160:163], v246 offset:5440
	v_or_b32_e32 v252, 0x20000, v2
	s_waitcnt lgkmcnt(1)
	global_store_dwordx4 v252, v[248:251], s[10:11] nt
	s_nop 0
	ds_read_b128 v[248:251], v246 offset:6528
	v_or_b32_e32 v3, 0x28000, v2
	s_waitcnt lgkmcnt(1)
	global_store_dwordx4 v3, v[160:163], s[10:11] nt
	s_nop 0
	ds_read_b128 v[160:163], v246 offset:7616
	v_or_b32_e32 v252, 0x30000, v2
	s_waitcnt lgkmcnt(1)
	global_store_dwordx4 v252, v[248:251], s[10:11] nt
	v_or_b32_e32 v3, 0x38000, v2
	s_waitcnt lgkmcnt(0)
	global_store_dwordx4 v3, v[160:163], s[10:11] nt
	s_mov_b32 s57, s24
	s_add_i32 s12, s12, 4
	s_cmp_eq_u32 s12, 32
	s_cbranch_scc1 .LBB1_22
